# LDS-transposed output stores: each half-wave writes 512 contiguous bytes of one channel plane; store tail without nops
# speedup vs baseline: 1.0063x; 1.0063x over previous
.LBB1_6:
	s_or_b64 exec, exec, s[10:11]
	v_lshrrev_b32_e32 v10, 6, v0
	v_lshlrev_b32_e32 v4, 7, v10
	v_lshrrev_b32_e32 v32, 1, v1
	v_lshl_or_b32 v71, s5, 9, v4
	v_lshl_or_b32 v68, v32, 2, v71
	v_mov_b32_e32 v69, 0
	s_waitcnt lgkmcnt(0)
	v_lshl_add_u64 v[4:5], v[68:69], 2, s[8:9]
	v_cmp_gt_u32_e32 vcc, 64, v0
	v_lshlrev_b32_e32 v6, 4, v1
	v_mov_b32_e32 v7, v69
	v_cndmask_b32_e32 v3, v5, v3, vcc
	v_cndmask_b32_e32 v2, v4, v2, vcc
	global_load_dword v70, v[2:3], off
	v_mad_u64_u32 v[2:3], s[6:7], v71, 12, s[6:7]
	v_lshlrev_b32_e32 v4, 2, v71
	v_mov_b32_e32 v5, v69
	s_movk_i32 s6, 0xfe00
	v_lshl_add_u64 v[4:5], s[8:9], 0, v[4:5]
	v_lshl_add_u64 v[8:9], v[2:3], 0, v[6:7]
	s_mov_b32 s7, -1
	v_lshl_add_u64 v[4:5], v[4:5], 0, v[6:7]
	v_lshl_add_u64 v[2:3], v[8:9], 0, s[6:7]
	v_cmp_gt_u32_e32 vcc, 32, v1
	v_lshlrev_b32_e32 v33, 12, v10
	v_add_u32_e32 v34, v33, v6
	v_cndmask_b32_e32 v3, v3, v5, vcc
	v_cndmask_b32_e32 v2, v2, v4, vcc
	global_load_dwordx4 v[2:5], v[2:3], off
	v_and_b32_e32 v72, 1, v0
	v_lshl_add_u32 v0, v32, 4, v33
	v_lshlrev_b32_e32 v73, 4, v32
	v_lshlrev_b32_e32 v74, 6, v72
	v_xor_b32_e32 v73, v73, v74
	v_lshl_add_u32 v73, v72, 11, v73
	v_lshl_add_u32 v73, v10, 12, v73
	v_and_b32_e32 v74, 31, v1
	v_lshrrev_b32_e32 v75, 5, v1
	v_lshl_or_b32 v76, v74, 2, v71
	v_lshlrev_b32_e32 v74, 4, v74
	v_lshlrev_b32_e32 v77, 6, v75
	v_xor_b32_e32 v74, v74, v77
	v_lshl_add_u32 v74, v75, 11, v74
	v_lshl_add_u32 v74, v10, 12, v74
	v_lshlrev_b32_e32 v77, 7, v71
	v_and_b32_e32 v77, 0xe000000, v77
	v_and_b32_e32 v76, 0x3fffc, v76
	v_lshlrev_b32_e32 v75, 21, v75
	v_or3_b32 v75, v77, v75, v76
	v_lshlrev_b32_e32 v75, 2, v75
	s_mul_i32 s6, s4, 0x138800
	s_mul_hi_i32 s5, s4, 0x138800
	s_add_u32 s2, s2, s6
	s_addc_u32 s3, s3, s5
	global_load_dwordx4 v[28:31], v[8:9], off offset:512
	s_waitcnt vmcnt(1)
	ds_write_b128 v34, v[2:5]
	ds_read_b128 v[4:7], v0
	v_lshlrev_b32_e32 v0, 4, v72
	s_waitcnt lgkmcnt(0)
	v_max_i32_e32 v1, 0, v4
	v_max_i32_e32 v2, 0, v5
	v_max_i32_e32 v3, 0, v6
	v_max_i32_e32 v8, 0, v7
	v_lshl_or_b32 v35, v1, 7, v0
	v_lshl_or_b32 v36, v2, 7, v0
	v_lshl_or_b32 v37, v3, 7, v0
	v_lshl_or_b32 v38, v8, 7, v0
	global_load_dwordx4 v[20:23], v35, s[2:3]
	global_load_dwordx4 v[16:19], v35, s[2:3] offset:32
	global_load_dwordx4 v[8:11], v35, s[2:3] offset:64
	global_load_dwordx4 v[64:67], v36, s[2:3]
	global_load_dwordx4 v[60:63], v36, s[2:3] offset:32
	global_load_dwordx4 v[56:59], v36, s[2:3] offset:64
	global_load_dwordx4 v[52:55], v37, s[2:3]
	global_load_dwordx4 v[48:51], v37, s[2:3] offset:32
	global_load_dwordx4 v[44:47], v37, s[2:3] offset:64
	global_load_dwordx4 v[24:27], v38, s[2:3]
	global_load_dwordx4 v[12:15], v38, s[2:3] offset:32
	global_load_dwordx4 v[0:3], v38, s[2:3] offset:64
	s_waitcnt vmcnt(12)
	ds_write_b128 v34, v[28:31] offset:1024
	v_mul_u32_u24_e32 v28, 48, v32
	v_cmp_lt_i32_e32 vcc, -1, v4
	v_add_u32_e32 v31, v33, v28
	v_mov_b32_e32 v28, 0
	s_and_saveexec_b64 s[2:3], vcc
	ds_read_b32 v28, v31 offset:512
	s_or_b64 exec, exec, s[2:3]
	s_and_saveexec_b64 s[2:3], vcc
	ds_read_b32 v69, v31 offset:516
	s_or_b64 exec, exec, s[2:3]
	v_mov_b32_e32 v29, 0
	v_mov_b32_e32 v4, 0
	s_and_saveexec_b64 s[2:3], vcc
	ds_read_b32 v4, v31 offset:520
	s_or_b64 exec, exec, s[2:3]
	s_waitcnt vmcnt(11) lgkmcnt(0)
	v_fma_mix_f32 v30, v28, v20, v29 op_sel_hi:[0,1,0]
	v_fma_mix_f32 v20, v28, v20, v29 op_sel:[0,1,0] op_sel_hi:[0,1,0]
	v_fma_mix_f32 v32, v28, v21, v29 op_sel_hi:[0,1,0]
	v_fma_mix_f32 v21, v28, v21, v29 op_sel:[0,1,0] op_sel_hi:[0,1,0]
	v_fma_mix_f32 v33, v28, v22, v29 op_sel_hi:[0,1,0]
	v_fma_mix_f32 v22, v28, v22, v29 op_sel:[0,1,0] op_sel_hi:[0,1,0]
	v_fma_mix_f32 v34, v28, v23, v29 op_sel_hi:[0,1,0]
	v_fma_mix_f32 v23, v28, v23, v29 op_sel:[0,1,0] op_sel_hi:[0,1,0]
	s_waitcnt vmcnt(10)
	v_fma_mix_f32 v28, v69, v16, v30 op_sel_hi:[0,1,0]
	v_fma_mix_f32 v16, v69, v16, v20 op_sel:[0,1,0] op_sel_hi:[0,1,0]
	v_fma_mix_f32 v20, v69, v17, v32 op_sel_hi:[0,1,0]
	v_cmp_lt_i32_e32 vcc, -1, v5
	v_fma_mix_f32 v17, v69, v17, v21 op_sel:[0,1,0] op_sel_hi:[0,1,0]
	v_fma_mix_f32 v21, v69, v18, v33 op_sel_hi:[0,1,0]
	v_fma_mix_f32 v18, v69, v18, v22 op_sel:[0,1,0] op_sel_hi:[0,1,0]
	v_fma_mix_f32 v22, v69, v19, v34 op_sel_hi:[0,1,0]
	v_fma_mix_f32 v19, v69, v19, v23 op_sel:[0,1,0] op_sel_hi:[0,1,0]
	s_waitcnt vmcnt(9)
	v_fma_mix_f32 v40, v4, v8, v28 op_sel_hi:[0,1,0]
	v_fma_mix_f32 v36, v4, v8, v16 op_sel:[0,1,0] op_sel_hi:[0,1,0]
	v_fma_mix_f32 v32, v4, v9, v20 op_sel_hi:[0,1,0]
	v_fma_mix_f32 v28, v4, v9, v17 op_sel:[0,1,0] op_sel_hi:[0,1,0]
	v_fma_mix_f32 v20, v4, v10, v21 op_sel_hi:[0,1,0]
	v_fma_mix_f32 v16, v4, v10, v18 op_sel:[0,1,0] op_sel_hi:[0,1,0]
	v_fma_mix_f32 v8, v4, v11, v22 op_sel_hi:[0,1,0]
	v_fma_mix_f32 v4, v4, v11, v19 op_sel:[0,1,0] op_sel_hi:[0,1,0]
	s_and_saveexec_b64 s[2:3], vcc
	ds_read_b32 v29, v31 offset:524
	s_or_b64 exec, exec, s[2:3]
	v_mov_b32_e32 v5, 0
	v_mov_b32_e32 v9, 0
	s_and_saveexec_b64 s[2:3], vcc
	ds_read_b32 v9, v31 offset:528
	s_or_b64 exec, exec, s[2:3]
	s_and_saveexec_b64 s[2:3], vcc
	ds_read_b32 v5, v31 offset:532
	s_or_b64 exec, exec, s[2:3]
	v_mov_b32_e32 v10, 0
	s_waitcnt vmcnt(8) lgkmcnt(0)
	v_fma_mix_f32 v18, v29, v65, v10 op_sel_hi:[0,1,0]
	v_fma_mix_f32 v17, v29, v64, v10 op_sel:[0,1,0] op_sel_hi:[0,1,0]
	v_fma_mix_f32 v21, v29, v66, v10 op_sel_hi:[0,1,0]
	v_fma_mix_f32 v11, v29, v64, v10 op_sel_hi:[0,1,0]
	v_fma_mix_f32 v19, v29, v65, v10 op_sel:[0,1,0] op_sel_hi:[0,1,0]
	s_waitcnt vmcnt(7)
	v_fma_mix_f32 v18, v9, v61, v18 op_sel_hi:[0,1,0]
	v_fma_mix_f32 v22, v29, v66, v10 op_sel:[0,1,0] op_sel_hi:[0,1,0]
	v_fma_mix_f32 v23, v29, v67, v10 op_sel_hi:[0,1,0]
	v_fma_mix_f32 v29, v29, v67, v10 op_sel:[0,1,0] op_sel_hi:[0,1,0]
	v_fma_mix_f32 v17, v9, v60, v17 op_sel:[0,1,0] op_sel_hi:[0,1,0]
	v_fma_mix_f32 v21, v9, v62, v21 op_sel_hi:[0,1,0]
	s_waitcnt vmcnt(6)
	v_fma_mix_f32 v33, v5, v57, v18 op_sel_hi:[0,1,0]
	v_cmp_lt_i32_e32 vcc, -1, v6
	v_mov_b32_e32 v18, 0
	v_fma_mix_f32 v11, v9, v60, v11 op_sel_hi:[0,1,0]
	v_fma_mix_f32 v19, v9, v61, v19 op_sel:[0,1,0] op_sel_hi:[0,1,0]
	v_fma_mix_f32 v22, v9, v62, v22 op_sel:[0,1,0] op_sel_hi:[0,1,0]
	v_fma_mix_f32 v23, v9, v63, v23 op_sel_hi:[0,1,0]
	v_fma_mix_f32 v30, v9, v63, v29 op_sel:[0,1,0] op_sel_hi:[0,1,0]
	v_fma_mix_f32 v37, v5, v56, v17 op_sel:[0,1,0] op_sel_hi:[0,1,0]
	s_nop 0
	v_fma_mix_f32 v41, v5, v56, v11 op_sel_hi:[0,1,0]
	v_fma_mix_f32 v29, v5, v57, v19 op_sel:[0,1,0] op_sel_hi:[0,1,0]
	v_fma_mix_f32 v21, v5, v58, v21 op_sel_hi:[0,1,0]
	v_fma_mix_f32 v17, v5, v58, v22 op_sel:[0,1,0] op_sel_hi:[0,1,0]
	v_fma_mix_f32 v9, v5, v59, v23 op_sel_hi:[0,1,0]
	v_fma_mix_f32 v5, v5, v59, v30 op_sel:[0,1,0] op_sel_hi:[0,1,0]
	s_and_saveexec_b64 s[2:3], vcc
	ds_read_b32 v18, v31 offset:536
	s_or_b64 exec, exec, s[2:3]
	s_and_saveexec_b64 s[2:3], vcc
	ds_read_b32 v10, v31 offset:540
	s_or_b64 exec, exec, s[2:3]
	v_mov_b32_e32 v11, 0
	v_mov_b32_e32 v6, 0
	s_and_saveexec_b64 s[2:3], vcc
	ds_read_b32 v6, v31 offset:544
	s_or_b64 exec, exec, s[2:3]
	s_waitcnt vmcnt(5) lgkmcnt(0)
	v_fma_mix_f32 v22, v18, v52, v11 op_sel:[0,1,0] op_sel_hi:[0,1,0]
	v_fma_mix_f32 v30, v18, v53, v11 op_sel:[0,1,0] op_sel_hi:[0,1,0]
	v_fma_mix_f32 v19, v18, v52, v11 op_sel_hi:[0,1,0]
	v_fma_mix_f32 v23, v18, v53, v11 op_sel_hi:[0,1,0]
	v_fma_mix_f32 v34, v18, v54, v11 op_sel_hi:[0,1,0]
	v_fma_mix_f32 v35, v18, v54, v11 op_sel:[0,1,0] op_sel_hi:[0,1,0]
	v_fma_mix_f32 v38, v18, v55, v11 op_sel_hi:[0,1,0]
	v_fma_mix_f32 v18, v18, v55, v11 op_sel:[0,1,0] op_sel_hi:[0,1,0]
	s_waitcnt vmcnt(4)
	v_fma_mix_f32 v22, v10, v48, v22 op_sel:[0,1,0] op_sel_hi:[0,1,0]
	v_fma_mix_f32 v30, v10, v49, v30 op_sel:[0,1,0] op_sel_hi:[0,1,0]
	v_cmp_lt_i32_e32 vcc, -1, v7
	v_fma_mix_f32 v19, v10, v48, v19 op_sel_hi:[0,1,0]
	v_fma_mix_f32 v23, v10, v49, v23 op_sel_hi:[0,1,0]
	v_fma_mix_f32 v39, v10, v50, v34 op_sel_hi:[0,1,0]
	v_fma_mix_f32 v35, v10, v50, v35 op_sel:[0,1,0] op_sel_hi:[0,1,0]
	v_fma_mix_f32 v43, v10, v51, v38 op_sel_hi:[0,1,0]
	v_fma_mix_f32 v48, v10, v51, v18 op_sel:[0,1,0] op_sel_hi:[0,1,0]
	s_waitcnt vmcnt(3)
	v_fma_mix_f32 v42, v6, v44, v19 op_sel_hi:[0,1,0]
	v_fma_mix_f32 v38, v6, v44, v22 op_sel:[0,1,0] op_sel_hi:[0,1,0]
	v_fma_mix_f32 v34, v6, v45, v23 op_sel_hi:[0,1,0]
	v_fma_mix_f32 v30, v6, v45, v30 op_sel:[0,1,0] op_sel_hi:[0,1,0]
	v_fma_mix_f32 v22, v6, v46, v39 op_sel_hi:[0,1,0]
	v_fma_mix_f32 v18, v6, v46, v35 op_sel:[0,1,0] op_sel_hi:[0,1,0]
	v_fma_mix_f32 v10, v6, v47, v43 op_sel_hi:[0,1,0]
	v_fma_mix_f32 v6, v6, v47, v48 op_sel:[0,1,0] op_sel_hi:[0,1,0]
	s_and_saveexec_b64 s[2:3], vcc
	ds_read_b32 v11, v31 offset:548
	s_or_b64 exec, exec, s[2:3]
	s_load_dwordx2 s[0:1], s[0:1], 0x18
	s_ashr_i32 s5, s4, 31
	v_mov_b32_e32 v7, 0
	v_mov_b32_e32 v19, 0
	s_and_saveexec_b64 s[2:3], vcc
	ds_read_b32 v19, v31 offset:552
	s_or_b64 exec, exec, s[2:3]
	s_and_saveexec_b64 s[2:3], vcc
	ds_read_b32 v7, v31 offset:556
	s_or_b64 exec, exec, s[2:3]
	v_mov_b32_e32 v23, 0
	s_waitcnt vmcnt(2) lgkmcnt(0)
	v_fma_mix_f32 v31, v11, v24, v23 op_sel_hi:[0,1,0]
	v_fma_mix_f32 v24, v11, v24, v23 op_sel:[0,1,0] op_sel_hi:[0,1,0]
	v_fma_mix_f32 v35, v11, v25, v23 op_sel_hi:[0,1,0]
	v_fma_mix_f32 v25, v11, v25, v23 op_sel:[0,1,0] op_sel_hi:[0,1,0]
	v_fma_mix_f32 v39, v11, v26, v23 op_sel_hi:[0,1,0]
	v_fma_mix_f32 v26, v11, v26, v23 op_sel:[0,1,0] op_sel_hi:[0,1,0]
	v_fma_mix_f32 v43, v11, v27, v23 op_sel_hi:[0,1,0]
	v_fma_mix_f32 v11, v11, v27, v23 op_sel:[0,1,0] op_sel_hi:[0,1,0]
	s_waitcnt vmcnt(1)
	v_fma_mix_f32 v23, v19, v12, v31 op_sel_hi:[0,1,0]
	s_lshl_b64 s[2:3], s[4:5], 24
	v_fma_mix_f32 v12, v19, v12, v24 op_sel:[0,1,0] op_sel_hi:[0,1,0]
	v_fma_mix_f32 v24, v19, v13, v35 op_sel_hi:[0,1,0]
	v_fma_mix_f32 v13, v19, v13, v25 op_sel:[0,1,0] op_sel_hi:[0,1,0]
	v_fma_mix_f32 v25, v19, v14, v39 op_sel_hi:[0,1,0]
	v_fma_mix_f32 v14, v19, v14, v26 op_sel:[0,1,0] op_sel_hi:[0,1,0]
	v_fma_mix_f32 v26, v19, v15, v43 op_sel_hi:[0,1,0]
	v_fma_mix_f32 v15, v19, v15, v11 op_sel:[0,1,0] op_sel_hi:[0,1,0]
	s_add_u32 s0, s0, s2
	s_addc_u32 s1, s1, s3
	s_add_u32 s2, s0, 0x100000
	s_addc_u32 s3, s1, 0
	s_add_u32 s4, s0, 0x200000
	s_addc_u32 s5, s1, 0
	s_add_u32 s6, s0, 0x300000
	s_addc_u32 s7, s1, 0
	s_add_u32 s8, s0, 0x400000
	s_addc_u32 s9, s1, 0
	s_add_u32 s10, s0, 0x500000
	s_addc_u32 s11, s1, 0
	s_add_u32 s12, s0, 0x600000
	s_addc_u32 s13, s1, 0
	s_add_u32 s14, s0, 0x700000
	s_addc_u32 s15, s1, 0
	s_waitcnt vmcnt(0)
	v_fma_mix_f32 v43, v7, v0, v23 op_sel_hi:[0,1,0]
	v_fma_mix_f32 v23, v7, v2, v25 op_sel_hi:[0,1,0]
	v_fma_mix_f32 v19, v7, v2, v14 op_sel:[0,1,0] op_sel_hi:[0,1,0]
	v_fma_mix_f32 v39, v7, v0, v12 op_sel:[0,1,0] op_sel_hi:[0,1,0]
	v_fma_mix_f32 v35, v7, v1, v24 op_sel_hi:[0,1,0]
	v_fma_mix_f32 v31, v7, v1, v13 op_sel:[0,1,0] op_sel_hi:[0,1,0]
	v_fma_mix_f32 v11, v7, v3, v26 op_sel_hi:[0,1,0]
	v_fma_mix_f32 v7, v7, v3, v15 op_sel:[0,1,0] op_sel_hi:[0,1,0]
	ds_write_b128 v73, v[40:43]
	ds_write_b128 v73, v[36:39] offset:512
	ds_write_b128 v73, v[32:35] offset:1024
	ds_write_b128 v73, v[28:31] offset:1536
	ds_read_b128 v[44:47], v74
	ds_read_b128 v[48:51], v74 offset:512
	ds_read_b128 v[52:55], v74 offset:1024
	ds_read_b128 v[56:59], v74 offset:1536
	ds_write_b128 v73, v[20:23]
	ds_write_b128 v73, v[16:19] offset:512
	ds_write_b128 v73, v[8:11] offset:1024
	ds_write_b128 v73, v[4:7] offset:1536
	s_waitcnt lgkmcnt(7)
	global_store_dwordx4 v75, v[44:47], s[0:1] nt
	s_waitcnt lgkmcnt(6)
	global_store_dwordx4 v75, v[48:51], s[2:3] nt
	s_waitcnt lgkmcnt(5)
	global_store_dwordx4 v75, v[52:55], s[4:5] nt
	s_waitcnt lgkmcnt(4)
	global_store_dwordx4 v75, v[56:59], s[6:7] nt
	ds_read_b128 v[60:63], v74
	ds_read_b128 v[64:67], v74 offset:512
	ds_read_b128 v[0:3], v74 offset:1024
	ds_read_b128 v[12:15], v74 offset:1536
	s_waitcnt lgkmcnt(3)
	global_store_dwordx4 v75, v[60:63], s[8:9] nt
	s_waitcnt lgkmcnt(2)
	global_store_dwordx4 v75, v[64:67], s[10:11] nt
	s_waitcnt lgkmcnt(1)
	global_store_dwordx4 v75, v[0:3], s[12:13] nt
	s_waitcnt lgkmcnt(0)
	global_store_dwordx4 v75, v[12:15], s[14:15] nt
	s_endpgm

	.amdhsa_kernel _Z6interpPKiPKfPK15HIP_vector_typeIjLj4EEPf
		.amdhsa_group_segment_fixed_size 16384
		.amdhsa_private_segment_fixed_size 0
		.amdhsa_kernarg_size 32
		.amdhsa_user_sgpr_count 2
		.amdhsa_user_sgpr_dispatch_ptr 0
		.amdhsa_user_sgpr_queue_ptr 0
		.amdhsa_user_sgpr_kernarg_segment_ptr 1
		.amdhsa_user_sgpr_dispatch_id 0
		.amdhsa_user_sgpr_kernarg_preload_length 0
		.amdhsa_user_sgpr_kernarg_preload_offset 0
		.amdhsa_user_sgpr_private_segment_size 0
		.amdhsa_uses_dynamic_stack 0
		.amdhsa_enable_private_segment 0
		.amdhsa_system_sgpr_workgroup_id_x 1
		.amdhsa_system_sgpr_workgroup_id_y 0
		.amdhsa_system_sgpr_workgroup_id_z 0
		.amdhsa_system_sgpr_workgroup_info 0
		.amdhsa_system_vgpr_workitem_id 0
		.amdhsa_next_free_vgpr 78
		.amdhsa_next_free_sgpr 16
		.amdhsa_accum_offset 80
		.amdhsa_reserve_vcc 1
		.amdhsa_float_round_mode_32 0
		.amdhsa_float_round_mode_16_64 0
		.amdhsa_float_denorm_mode_32 3
		.amdhsa_float_denorm_mode_16_64 3
		.amdhsa_dx10_clamp 1
		.amdhsa_ieee_mode 1
		.amdhsa_fp16_overflow 0
		.amdhsa_tg_split 0
		.amdhsa_exception_fp_ieee_invalid_op 0
		.amdhsa_exception_fp_denorm_src 0
		.amdhsa_exception_fp_ieee_div_zero 0
		.amdhsa_exception_fp_ieee_overflow 0
		.amdhsa_exception_fp_ieee_underflow 0
		.amdhsa_exception_fp_ieee_inexact 0
		.amdhsa_exception_int_div_zero 0
	.end_amdhsa_kernel

amdhsa.kernels:
  - .agpr_count:     0
    .args:
      - .actual_access:  read_only
        .address_space:  global
        .offset:         0
        .size:           8
        .value_kind:     global_buffer
      - .actual_access:  write_only
        .address_space:  global
        .offset:         8
        .size:           8
        .value_kind:     global_buffer
      - .address_space:  global
        .offset:         16
        .size:           8
        .value_kind:     global_buffer
      - .address_space:  global
        .offset:         24
        .size:           8
        .value_kind:     global_buffer
    .group_segment_fixed_size: 0
    .kernarg_segment_align: 8
    .kernarg_segment_size: 32
    .language:       OpenCL C
    .language_version:
      - 2
      - 0
    .max_flat_workgroup_size: 256
    .name:           _Z13convert_tablePKfP15HIP_vector_typeIjLj4EEPKiS0_
    .private_segment_fixed_size: 0
    .sgpr_count:     18
    .sgpr_spill_count: 0
    .symbol:         _Z13convert_tablePKfP15HIP_vector_typeIjLj4EEPKiS0_.kd
    .uniform_work_group_size: 1
    .uses_dynamic_stack: false
    .vgpr_count:     16
    .vgpr_spill_count: 0
    .wavefront_size: 64
  - .agpr_count:     0
    .args:
      - .address_space:  global
        .offset:         0
        .size:           8
        .value_kind:     global_buffer
      - .address_space:  global
        .offset:         8
        .size:           8
        .value_kind:     global_buffer
      - .actual_access:  read_only
        .address_space:  global
        .offset:         16
        .size:           8
        .value_kind:     global_buffer
      - .address_space:  global
        .offset:         24
        .size:           8
        .value_kind:     global_buffer
    .group_segment_fixed_size: 16384
    .kernarg_segment_align: 8
    .kernarg_segment_size: 32
    .language:       OpenCL C
    .language_version:
      - 2
      - 0
    .max_flat_workgroup_size: 256
    .name:           _Z6interpPKiPKfPK15HIP_vector_typeIjLj4EEPf
    .private_segment_fixed_size: 0
    .sgpr_count:     22
    .sgpr_spill_count: 0
    .symbol:         _Z6interpPKiPKfPK15HIP_vector_typeIjLj4EEPf.kd
    .uniform_work_group_size: 1
    .uses_dynamic_stack: false
    .vgpr_count:     78
    .vgpr_spill_count: 0
    .wavefront_size: 64
